# P10 K-loop: first-iteration SP1 and (non-first units) SP2 waits skipped; they only retired loads already drained by the epilogue
# baseline (speedup 1.0000x reference)
; #define PG8_STAGE(bufoff, gbase, voff) do { _Pragma("unroll") for (int _i = 0; _i < 2; ++_i) \
;         __builtin_amdgcn_global_load_lds((const unsigned*)((const char*)(gbase) + (voff)[_i]), (PG8_LAS unsigned*)(lds + (bufoff) + ldsw + _i * 8192), 16, 0, 0); } while (0)
; #define PG8_LDA(dst, b, h) do { _Pragma("unroll") for (int m = 0; m < 4; ++m) _Pragma("unroll") for (int k = 0; k < 2; ++k) dst[m][k] = *(const PG8_LAS bf16x8*)(lds + PG8_SA(b, h) + aoff + m * 2048 + k * 1024); } while (0)
; #define PG8_LDB(dst, b, h) do { _Pragma("unroll") for (int n = 0; n < 2; ++n) _Pragma("unroll") for (int k = 0; k < 2; ++k) dst[n][k] = *(const PG8_LAS bf16x8*)(lds + PG8_SB(b, h) + boff + n * 2048 + k * 1024); } while (0)
; #define PG8_WAIT_V(n) asm volatile("s_waitcnt vmcnt(" #n ")" ::: "memory")
; #define PG8_WAIT_L(n) asm volatile("s_waitcnt lgkmcnt(" #n ")" ::: "memory")
; #define PG8_BAR __builtin_amdgcn_s_barrier()
; #define PG8_SCHED __builtin_amdgcn_sched_barrier(0)
; template <class Epi, class Sched, bool ALIGN_EPI = false, bool SP2 = false, bool F8 = false, bool GATHER = false>
; __device__ __forceinline__ void gemm_phase(PG8_LAS unsigned char* lds, const Gemm g, const Sched& S, const Epi& E) {
;     ...
;             PG8_LDB(B0, 0, 0); PG8_LDB(B1, 0, 1); PG8_SCHED; PG8_LDA(At, 0, 0); PG8_STAGE(PG8_SA(1, 1), a1, vo[1]);
;             PG8_WAIT_V(8); PG8_WAIT_L(0); PG8_BAR; PG8_MMA(0, 0, At, B0); PG8_MMA(0, 1, At, B1); PG8_BAR; PG8_SCHED;
;             PG8_LDA(At, 0, 1); PG8_STAGE(PG8_SB(0, 0), b2, voffB); PG8_STAGE(PG8_SB(0, 1), b2 + hstep, voffB); PG8_STAGE(PG8_SA(0, 0), a2, s0);
;             PG8_WAIT_V(8); PG8_WAIT_L(0); PG8_BAR; PG8_MMA(1, 0, At, B0); PG8_MMA(1, 1, At, B1); PG8_BAR; PG8_SCHED;
;             PG8_LDB(B0, 1, 0); PG8_LDB(B1, 1, 1); PG8_SCHED; PG8_LDA(At, 1, 0); PG8_STAGE(PG8_SA(0, 1), a2, s1);
;             PG8_WAIT_V(8); PG8_WAIT_L(0); PG8_BAR; PG8_MMA(0, 0, At, B0); PG8_MMA(0, 1, At, B1); PG8_BAR; PG8_SCHED;
.Lw10_skip:
	s_waitcnt lgkmcnt(0)
	s_barrier
	s_setprio 1
	s_waitcnt lgkmcnt(0)
	v_mfma_scale_f32_16x16x128_f8f6f4 v[158:161], v[26:33], v[178:185], v[158:161], v199, v199 op_sel_hi:[0,0,0]
	v_mfma_scale_f32_16x16x128_f8f6f4 v[154:157], v[18:25], v[178:185], v[154:157], v199, v199 op_sel_hi:[0,0,0]
	v_mfma_scale_f32_16x16x128_f8f6f4 v[146:149], v[26:33], v[206:213], v[146:149], v199, v199 op_sel_hi:[0,0,0]
	v_mfma_scale_f32_16x16x128_f8f6f4 v[138:141], v[18:25], v[206:213], v[138:141], v199, v199 op_sel_hi:[0,0,0]
	v_mfma_scale_f32_16x16x128_f8f6f4 v[130:133], v[26:33], v[214:221], v[130:133], v199, v199 op_sel_hi:[0,0,0]
	v_mfma_scale_f32_16x16x128_f8f6f4 v[122:125], v[18:25], v[214:221], v[122:125], v199, v199 op_sel_hi:[0,0,0]
	v_mfma_scale_f32_16x16x128_f8f6f4 v[114:117], v[26:33], v[222:229], v[114:117], v199, v199 op_sel_hi:[0,0,0]
	v_mfma_scale_f32_16x16x128_f8f6f4 v[106:109], v[18:25], v[222:229], v[106:109], v199, v199 op_sel_hi:[0,0,0]
	s_setprio 0
	s_setprio 1
	v_mfma_scale_f32_16x16x128_f8f6f4 v[150:153], v[10:17], v[178:185], v[150:153], v199, v199 op_sel_hi:[0,0,0]
	v_mfma_scale_f32_16x16x128_f8f6f4 v[142:145], v[2:9], v[178:185], v[142:145], v199, v199 op_sel_hi:[0,0,0]
	v_mfma_scale_f32_16x16x128_f8f6f4 v[134:137], v[10:17], v[206:213], v[134:137], v199, v199 op_sel_hi:[0,0,0]
	v_mfma_scale_f32_16x16x128_f8f6f4 v[126:129], v[2:9], v[206:213], v[126:129], v199, v199 op_sel_hi:[0,0,0]
	v_mfma_scale_f32_16x16x128_f8f6f4 v[118:121], v[10:17], v[214:221], v[118:121], v199, v199 op_sel_hi:[0,0,0]
	v_mfma_scale_f32_16x16x128_f8f6f4 v[110:113], v[2:9], v[214:221], v[110:113], v199, v199 op_sel_hi:[0,0,0]
	v_mfma_scale_f32_16x16x128_f8f6f4 v[102:105], v[10:17], v[222:229], v[102:105], v199, v199 op_sel_hi:[0,0,0]
	v_mfma_scale_f32_16x16x128_f8f6f4 v[98:101], v[2:9], v[222:229], v[98:101], v199, v199 op_sel_hi:[0,0,0]
	s_setprio 0
	s_barrier
	s_add_i32 s72, s60, s1
	v_lshl_add_u64 v[178:179], s[54:55], 0, v[164:165]
	s_mov_b32 m0, s72
	ds_read_b128 v[206:209], v198 offset:16384
	ds_read_b128 v[210:213], v198 offset:17408
	ds_read_b128 v[214:217], v198 offset:18432
	ds_read_b128 v[218:221], v198 offset:19456
	ds_read_b128 v[222:225], v198 offset:20480
	ds_read_b128 v[226:229], v198 offset:21504
	ds_read_b128 v[230:233], v198 offset:22528
	ds_read_b128 v[234:237], v198 offset:23552
	global_load_lds_dwordx4 v[178:179], off
	s_add_i32 m0, s72, 0x2000
	s_add_u32 s72, s54, 0x40000
	v_lshl_add_u64 v[180:181], s[54:55], 0, v[162:163]
	s_addc_u32 s73, s55, 0
	s_add_i32 s74, s61, s1
	global_load_lds_dwordx4 v[180:181], off
	v_lshl_add_u64 v[182:183], s[72:73], 0, v[164:165]
	s_mov_b32 m0, s74
	v_mov_b32_e32 v239, v167
	global_load_lds_dwordx4 v[182:183], off
	v_lshl_add_u64 v[182:183], s[72:73], 0, v[162:163]
	s_add_i32 m0, s74, 0x2000
	v_lshl_add_u64 v[184:185], s[56:57], 0, v[166:167]
	global_load_lds_dwordx4 v[182:183], off
	s_mov_b32 m0, s11
	v_lshl_add_u64 v[182:183], s[56:57], 0, v[238:239]
	global_load_lds_dwordx4 v166, s[56:57]
	s_mov_b32 m0, s33
	s_nop 0
	global_load_lds_dwordx4 v238, s[56:57]
	s_cmp_lg_u32 s71, -2
	s_cbranch_scc1 .Lw10b_wait
	s_cmp_lt_u32 s39, 2
	s_cbranch_scc0 .Lw10b_skip
.Lw10b_wait:
	s_waitcnt vmcnt(8)
.Lw10b_skip:
	s_waitcnt lgkmcnt(0)
	s_barrier
	s_setprio 1
	s_waitcnt lgkmcnt(0)
	v_mfma_scale_f32_16x16x128_f8f6f4 v[94:97], v[26:33], v[206:213], v[94:97], v199, v199 op_sel_hi:[0,0,0]
	v_mfma_scale_f32_16x16x128_f8f6f4 v[90:93], v[18:25], v[206:213], v[90:93], v199, v199 op_sel_hi:[0,0,0]
	v_mfma_scale_f32_16x16x128_f8f6f4 v[82:85], v[26:33], v[214:221], v[82:85], v199, v199 op_sel_hi:[0,0,0]
	v_mfma_scale_f32_16x16x128_f8f6f4 v[74:77], v[18:25], v[214:221], v[74:77], v199, v199 op_sel_hi:[0,0,0]
	v_mfma_scale_f32_16x16x128_f8f6f4 v[66:69], v[26:33], v[222:229], v[66:69], v199, v199 op_sel_hi:[0,0,0]
	v_mfma_scale_f32_16x16x128_f8f6f4 v[58:61], v[18:25], v[222:229], v[58:61], v199, v199 op_sel_hi:[0,0,0]
	v_mfma_scale_f32_16x16x128_f8f6f4 v[50:53], v[26:33], v[230:237], v[50:53], v199, v199 op_sel_hi:[0,0,0]
	v_mfma_scale_f32_16x16x128_f8f6f4 v[42:45], v[18:25], v[230:237], v[42:45], v199, v199 op_sel_hi:[0,0,0]
	s_setprio 0
	s_setprio 1
	v_mfma_scale_f32_16x16x128_f8f6f4 v[86:89], v[10:17], v[206:213], v[86:89], v199, v199 op_sel_hi:[0,0,0]
	v_mfma_scale_f32_16x16x128_f8f6f4 v[78:81], v[2:9], v[206:213], v[78:81], v199, v199 op_sel_hi:[0,0,0]
	v_mfma_scale_f32_16x16x128_f8f6f4 v[70:73], v[10:17], v[214:221], v[70:73], v199, v199 op_sel_hi:[0,0,0]
	v_mfma_scale_f32_16x16x128_f8f6f4 v[62:65], v[2:9], v[214:221], v[62:65], v199, v199 op_sel_hi:[0,0,0]
	v_mfma_scale_f32_16x16x128_f8f6f4 v[54:57], v[10:17], v[222:229], v[54:57], v199, v199 op_sel_hi:[0,0,0]
	v_mfma_scale_f32_16x16x128_f8f6f4 v[46:49], v[2:9], v[222:229], v[46:49], v199, v199 op_sel_hi:[0,0,0]
	v_mfma_scale_f32_16x16x128_f8f6f4 v[38:41], v[10:17], v[230:237], v[38:41], v199, v199 op_sel_hi:[0,0,0]
	v_mfma_scale_f32_16x16x128_f8f6f4 v[34:37], v[2:9], v[230:237], v[34:37], v199, v199 op_sel_hi:[0,0,0]
	s_setprio 0
	s_barrier
	s_add_i32 s72, 0, 0x18000
	s_add_i32 s73, 0, 0x1c000
	v_add_u32_e32 v14, s72, v194
	v_add_u32_e32 v30, s73, v194
	ds_read_b128 v[2:5], v14
	ds_read_b128 v[6:9], v14 offset:1024
	ds_read_b128 v[10:13], v14 offset:2048
	ds_read_b128 v[14:17], v14 offset:3072
	ds_read_b128 v[18:21], v30
	ds_read_b128 v[22:25], v30 offset:1024
	ds_read_b128 v[26:29], v30 offset:2048
	ds_read_b128 v[30:33], v30 offset:3072
	s_mov_b32 m0, s34
	ds_read_b128 v[206:209], v198 offset:32768
	ds_read_b128 v[210:213], v198 offset:33792
	ds_read_b128 v[214:217], v198 offset:34816
	ds_read_b128 v[218:221], v198 offset:35840
	ds_read_b128 v[222:225], v198 offset:36864
	ds_read_b128 v[226:229], v198 offset:37888
	ds_read_b128 v[230:233], v198 offset:38912
	ds_read_b128 v[234:237], v198 offset:39936
	global_load_lds_dwordx4 v171, s[56:57]
	s_mov_b32 m0, s35
	s_nop 0
	global_load_lds_dwordx4 v173, s[56:57]
	s_waitcnt vmcnt(8)
	s_waitcnt lgkmcnt(0)
	s_barrier
; #define PG8_STAGE(bufoff, gbase, voff) do { _Pragma("unroll") for (int _i = 0; _i < 2; ++_i) \
;         __builtin_amdgcn_global_load_lds((const unsigned*)((const char*)(gbase) + (voff)[_i]), (PG8_LAS unsigned*)(lds + (bufoff) + ldsw + _i * 8192), 16, 0, 0); } while (0)
; #define PG8_LDA(dst, b, h) do { _Pragma("unroll") for (int m = 0; m < 4; ++m) _Pragma("unroll") for (int k = 0; k < 2; ++k) dst[m][k] = *(const PG8_LAS bf16x8*)(lds + PG8_SA(b, h) + aoff + m * 2048 + k * 1024); } while (0)
; #define PG8_WAIT_V(n) asm volatile("s_waitcnt vmcnt(" #n ")" ::: "memory")
; #define PG8_WAIT_L(n) asm volatile("s_waitcnt lgkmcnt(" #n ")" ::: "memory")
; #define PG8_BAR __builtin_amdgcn_s_barrier()
; #define PG8_SCHED __builtin_amdgcn_sched_barrier(0)
; template <class Epi, class Sched, bool ALIGN_EPI = false, bool SP2 = false, bool F8 = false, bool GATHER = false>
; __device__ __forceinline__ void gemm_phase(PG8_LAS unsigned char* lds, const Gemm g, const Sched& S, const Epi& E) {
;     ...
;             PG8_WAIT_V(8); PG8_WAIT_L(0); PG8_BAR; PG8_MMA(0, 0, At, B0); PG8_MMA(0, 1, At, B1); PG8_BAR; PG8_SCHED;
;             PG8_LDA(At, 1, 1); PG8_STAGE(PG8_SB(1, 0), b3, voffB); PG8_STAGE(PG8_SB(1, 1), b3 + hstep, voffB); PG8_STAGE(PG8_SA(1, 0), a3, s0);
;             PG8_WAIT_V(8); PG8_WAIT_L(0); PG8_BAR; PG8_MMA(1, 0, At, B0); PG8_MMA(1, 1, At, B1); PG8_BAR; PG8_SCHED;
;     ...
;         if constexpr (F8) asm volatile("s_nop 15\n\ts_nop 7" ::: "memory");
;         if constexpr (ALIGN_EPI) { if (wr == 0) PG8_BAR; }
	s_setprio 1
	s_waitcnt lgkmcnt(0)
	v_mfma_scale_f32_16x16x128_f8f6f4 v[158:161], v[2:9], v[206:213], v[158:161], v199, v199 op_sel_hi:[0,0,0]
	v_mfma_scale_f32_16x16x128_f8f6f4 v[154:157], v[10:17], v[206:213], v[154:157], v199, v199 op_sel_hi:[0,0,0]
	v_mfma_scale_f32_16x16x128_f8f6f4 v[146:149], v[2:9], v[214:221], v[146:149], v199, v199 op_sel_hi:[0,0,0]
	v_mfma_scale_f32_16x16x128_f8f6f4 v[138:141], v[10:17], v[214:221], v[138:141], v199, v199 op_sel_hi:[0,0,0]
	v_mfma_scale_f32_16x16x128_f8f6f4 v[130:133], v[2:9], v[222:229], v[130:133], v199, v199 op_sel_hi:[0,0,0]
	v_mfma_scale_f32_16x16x128_f8f6f4 v[122:125], v[10:17], v[222:229], v[122:125], v199, v199 op_sel_hi:[0,0,0]
	v_mfma_scale_f32_16x16x128_f8f6f4 v[114:117], v[2:9], v[230:237], v[114:117], v199, v199 op_sel_hi:[0,0,0]
	v_mfma_scale_f32_16x16x128_f8f6f4 v[106:109], v[10:17], v[230:237], v[106:109], v199, v199 op_sel_hi:[0,0,0]
	s_setprio 0
	s_setprio 1
	v_mfma_scale_f32_16x16x128_f8f6f4 v[150:153], v[18:25], v[206:213], v[150:153], v199, v199 op_sel_hi:[0,0,0]
	v_mfma_scale_f32_16x16x128_f8f6f4 v[142:145], v[26:33], v[206:213], v[142:145], v199, v199 op_sel_hi:[0,0,0]
	v_mfma_scale_f32_16x16x128_f8f6f4 v[134:137], v[18:25], v[214:221], v[134:137], v199, v199 op_sel_hi:[0,0,0]
	v_mfma_scale_f32_16x16x128_f8f6f4 v[126:129], v[26:33], v[214:221], v[126:129], v199, v199 op_sel_hi:[0,0,0]
	v_mfma_scale_f32_16x16x128_f8f6f4 v[118:121], v[18:25], v[222:229], v[118:121], v199, v199 op_sel_hi:[0,0,0]
	v_mfma_scale_f32_16x16x128_f8f6f4 v[110:113], v[26:33], v[222:229], v[110:113], v199, v199 op_sel_hi:[0,0,0]
	v_mfma_scale_f32_16x16x128_f8f6f4 v[102:105], v[18:25], v[230:237], v[102:105], v199, v199 op_sel_hi:[0,0,0]
	v_mfma_scale_f32_16x16x128_f8f6f4 v[98:101], v[26:33], v[230:237], v[98:101], v199, v199 op_sel_hi:[0,0,0]
	s_setprio 0
	s_barrier
	s_add_i32 s56, s72, s1
	v_lshl_add_u64 v[178:179], v[178:179], 0, s[22:23]
	s_mov_b32 m0, s56
	ds_read_b128 v[206:209], v198 offset:49152
	ds_read_b128 v[210:213], v198 offset:50176
	ds_read_b128 v[214:217], v198 offset:51200
	ds_read_b128 v[218:221], v198 offset:52224
	ds_read_b128 v[222:225], v198 offset:53248
	ds_read_b128 v[226:229], v198 offset:54272
	ds_read_b128 v[230:233], v198 offset:55296
	ds_read_b128 v[234:237], v198 offset:56320
	global_load_lds_dwordx4 v[178:179], off
	s_add_i32 m0, s56, 0x2000
	s_add_u32 s54, s54, 0x40080
	v_lshl_add_u64 v[178:179], v[180:181], 0, s[22:23]
	s_addc_u32 s55, s55, 0
	s_add_i32 s56, s73, s1
	global_load_lds_dwordx4 v[178:179], off
	v_lshl_add_u64 v[178:179], s[54:55], 0, v[164:165]
	s_mov_b32 m0, s56
	s_nop 0
	global_load_lds_dwordx4 v[178:179], off
	v_lshl_add_u64 v[178:179], s[54:55], 0, v[162:163]
	s_add_i32 m0, s56, 0x2000
	s_nop 0
	global_load_lds_dwordx4 v[178:179], off
	v_lshl_add_u64 v[178:179], v[184:185], 0, s[22:23]
	s_mov_b32 m0, s58
	s_nop 0
	global_load_lds_dwordx4 v[178:179], off
	v_lshl_add_u64 v[178:179], v[182:183], 0, s[22:23]
	s_mov_b32 m0, s59
	s_nop 0
	global_load_lds_dwordx4 v[178:179], off
	s_waitcnt vmcnt(8)
	s_waitcnt lgkmcnt(0)
	s_barrier
	s_setprio 1
	s_waitcnt lgkmcnt(0)
	v_mfma_scale_f32_16x16x128_f8f6f4 v[94:97], v[2:9], v[206:213], v[94:97], v199, v199 op_sel_hi:[0,0,0]
	v_mfma_scale_f32_16x16x128_f8f6f4 v[90:93], v[10:17], v[206:213], v[90:93], v199, v199 op_sel_hi:[0,0,0]
	v_mfma_scale_f32_16x16x128_f8f6f4 v[82:85], v[2:9], v[214:221], v[82:85], v199, v199 op_sel_hi:[0,0,0]
	v_mfma_scale_f32_16x16x128_f8f6f4 v[74:77], v[10:17], v[214:221], v[74:77], v199, v199 op_sel_hi:[0,0,0]
	v_mfma_scale_f32_16x16x128_f8f6f4 v[66:69], v[2:9], v[222:229], v[66:69], v199, v199 op_sel_hi:[0,0,0]
	v_mfma_scale_f32_16x16x128_f8f6f4 v[58:61], v[10:17], v[222:229], v[58:61], v199, v199 op_sel_hi:[0,0,0]
	v_mfma_scale_f32_16x16x128_f8f6f4 v[50:53], v[2:9], v[230:237], v[50:53], v199, v199 op_sel_hi:[0,0,0]
	v_mfma_scale_f32_16x16x128_f8f6f4 v[42:45], v[10:17], v[230:237], v[42:45], v199, v199 op_sel_hi:[0,0,0]
	s_setprio 0
	s_setprio 1
	v_mfma_scale_f32_16x16x128_f8f6f4 v[86:89], v[18:25], v[206:213], v[86:89], v199, v199 op_sel_hi:[0,0,0]
	v_mfma_scale_f32_16x16x128_f8f6f4 v[78:81], v[26:33], v[206:213], v[78:81], v199, v199 op_sel_hi:[0,0,0]
	v_mfma_scale_f32_16x16x128_f8f6f4 v[70:73], v[18:25], v[214:221], v[70:73], v199, v199 op_sel_hi:[0,0,0]
	v_mfma_scale_f32_16x16x128_f8f6f4 v[62:65], v[26:33], v[214:221], v[62:65], v199, v199 op_sel_hi:[0,0,0]
	v_mfma_scale_f32_16x16x128_f8f6f4 v[54:57], v[18:25], v[222:229], v[54:57], v199, v199 op_sel_hi:[0,0,0]
	v_mfma_scale_f32_16x16x128_f8f6f4 v[46:49], v[26:33], v[222:229], v[46:49], v199, v199 op_sel_hi:[0,0,0]
	v_mfma_scale_f32_16x16x128_f8f6f4 v[38:41], v[18:25], v[230:237], v[38:41], v199, v199 op_sel_hi:[0,0,0]
	v_mfma_scale_f32_16x16x128_f8f6f4 v[34:37], v[26:33], v[230:237], v[34:37], v199, v199 op_sel_hi:[0,0,0]
	s_setprio 0
	s_barrier
	s_add_i32 s71, s71, 2
	s_add_u32 s4, s4, 0x100
	s_addc_u32 s5, s5, 0
	s_cmp_gt_u32 s71, 13
	s_cbranch_scc0 .LBB0_1073
	s_nop 15
	s_nop 7
	s_and_b64 vcc, exec, s[36:37]
	s_cbranch_vccz .LBB0_1076
	s_barrier
